# baseline (speedup 1.0000x reference)
.LBB1_151:
	v_add_u32_e32 v58, s19, v59
	v_min_i32_e32 v8, s18, v58
	v_lshlrev_b32_e32 v8, 3, v8
	ds_read_b64 v[66:67], v8 offset:32768
	v_add_u32_e32 v87, 4, v58
	v_add_u32_e32 v86, 8, v58
	v_min_i32_e32 v8, s18, v87
	v_min_i32_e32 v9, s18, v86
	v_add_u32_e32 v85, 12, v58
	v_lshlrev_b32_e32 v8, 3, v8
	v_lshlrev_b32_e32 v9, 3, v9
	v_min_i32_e32 v10, s18, v85
	v_lshlrev_b32_e32 v10, 3, v10
	ds_read_b64 v[64:65], v8 offset:32768
	ds_read_b64 v[62:63], v9 offset:32768
	ds_read_b64 v[60:61], v10 offset:32768
	s_waitcnt lgkmcnt(3)
	v_ashrrev_i32_e32 v9, 31, v67
	v_mov_b32_e32 v8, v67
	v_lshlrev_b64 v[8:9], 9, v[8:9]
	v_lshl_add_u64 v[8:9], v[40:41], 0, v[8:9]
	global_load_dwordx4 v[88:91], v[8:9], off
	s_nop 0
	global_load_dwordx4 v[8:11], v[8:9], off offset:256
	s_waitcnt lgkmcnt(2)
	v_ashrrev_i32_e32 v13, 31, v65
	v_mov_b32_e32 v12, v65
	v_lshlrev_b64 v[12:13], 9, v[12:13]
	v_lshl_add_u64 v[12:13], v[40:41], 0, v[12:13]
	global_load_dwordx4 v[32:35], v[12:13], off
	global_load_dwordx4 v[16:19], v[12:13], off offset:256
	s_waitcnt lgkmcnt(1)
	v_ashrrev_i32_e32 v13, 31, v63
	v_mov_b32_e32 v12, v63
	v_lshlrev_b64 v[12:13], 9, v[12:13]
	v_lshl_add_u64 v[12:13], v[40:41], 0, v[12:13]
	global_load_dwordx4 v[28:31], v[12:13], off
	global_load_dwordx4 v[20:23], v[12:13], off offset:256
	s_waitcnt lgkmcnt(0)
	v_ashrrev_i32_e32 v13, 31, v61
	v_mov_b32_e32 v12, v61
	v_lshlrev_b64 v[12:13], 9, v[12:13]
	v_lshl_add_u64 v[12:13], v[40:41], 0, v[12:13]
	global_load_dwordx4 v[24:27], v[12:13], off
	s_nop 0
	global_load_dwordx4 v[12:15], v[12:13], off offset:256
	v_cmp_le_i32_e32 vcc, s17, v58
	s_nor_b64 s[12:13], s[2:3], vcc
	s_waitcnt vmcnt(7)
	v_fma_mix_f32 v61, v0, v88, 0 op_sel_hi:[0,1,0]
	v_fma_mix_f32 v61, v1, v88, v61 op_sel:[0,1,0] op_sel_hi:[0,1,0]
	v_fma_mix_f32 v61, v2, v89, v61 op_sel_hi:[0,1,0]
	v_fma_mix_f32 v61, v3, v89, v61 op_sel:[0,1,0] op_sel_hi:[0,1,0]
	v_fma_mix_f32 v61, v4, v90, v61 op_sel_hi:[0,1,0]
	v_fma_mix_f32 v61, v5, v90, v61 op_sel:[0,1,0] op_sel_hi:[0,1,0]
	v_fma_mix_f32 v61, v6, v91, v61 op_sel_hi:[0,1,0]
	v_fma_mix_f32 v61, v7, v91, v61 op_sel:[0,1,0] op_sel_hi:[0,1,0]
	s_nop 1
	v_add_f32_dpp v61, v61, v61 quad_perm:[1,0,3,2] row_mask:0xf bank_mask:0xf
	v_max_f32_e32 v61, 0xc1200000, v61
	v_min_f32_e32 v61, 0x41200000, v61
	v_mul_f32_e32 v61, 0x3fb8aa3b, v61
	v_exp_f32_e32 v61, v61
	s_nop 0
	v_cndmask_b32_e64 v58, v61, 0, vcc
	s_and_saveexec_b64 s[10:11], s[12:13]
	s_cbranch_execz .LBB1_156
	s_andn2_b64 vcc, exec, s[6:7]
	s_mov_b64 s[12:13], -1
	s_cbranch_vccnz .LBB1_154
	s_mov_b64 s[12:13], 0
	ds_write_b32 v83, v58

.LBB1_156:
	s_or_b64 exec, exec, s[10:11]
	s_waitcnt vmcnt(5)
	v_fma_mix_f32 v61, v0, v32, 0 op_sel_hi:[0,1,0]
	v_fma_mix_f32 v32, v1, v32, v61 op_sel:[0,1,0] op_sel_hi:[0,1,0]
	v_fma_mix_f32 v32, v2, v33, v32 op_sel_hi:[0,1,0]
	v_fma_mix_f32 v32, v3, v33, v32 op_sel:[0,1,0] op_sel_hi:[0,1,0]
	v_fma_mix_f32 v32, v4, v34, v32 op_sel_hi:[0,1,0]
	v_fma_mix_f32 v32, v5, v34, v32 op_sel:[0,1,0] op_sel_hi:[0,1,0]
	v_fma_mix_f32 v32, v6, v35, v32 op_sel_hi:[0,1,0]
	v_fma_mix_f32 v32, v7, v35, v32 op_sel:[0,1,0] op_sel_hi:[0,1,0]
	v_cmp_le_i32_e32 vcc, s17, v87
	s_nor_b64 s[12:13], s[2:3], vcc
	v_add_f32_dpp v32, v32, v32 quad_perm:[1,0,3,2] row_mask:0xf bank_mask:0xf
	v_max_f32_e32 v32, 0xc1200000, v32
	v_min_f32_e32 v32, 0x41200000, v32
	v_mul_f32_e32 v32, 0x3fb8aa3b, v32
	v_exp_f32_e32 v32, v32
	s_nop 0
	v_cndmask_b32_e64 v32, v32, 0, vcc
	s_and_saveexec_b64 s[10:11], s[12:13]
	s_cbranch_execz .LBB1_161
	s_andn2_b64 vcc, exec, s[6:7]
	s_mov_b64 s[12:13], -1
	s_cbranch_vccnz .LBB1_159
	s_mov_b64 s[12:13], 0
	ds_write_b32 v83, v32 offset:128

.LBB1_161:
	s_or_b64 exec, exec, s[10:11]
	s_waitcnt vmcnt(3)
	v_fma_mix_f32 v33, v0, v28, 0 op_sel_hi:[0,1,0]
	v_fma_mix_f32 v28, v1, v28, v33 op_sel:[0,1,0] op_sel_hi:[0,1,0]
	v_fma_mix_f32 v28, v2, v29, v28 op_sel_hi:[0,1,0]
	v_fma_mix_f32 v28, v3, v29, v28 op_sel:[0,1,0] op_sel_hi:[0,1,0]
	v_fma_mix_f32 v28, v4, v30, v28 op_sel_hi:[0,1,0]
	v_fma_mix_f32 v28, v5, v30, v28 op_sel:[0,1,0] op_sel_hi:[0,1,0]
	v_fma_mix_f32 v28, v6, v31, v28 op_sel_hi:[0,1,0]
	v_fma_mix_f32 v28, v7, v31, v28 op_sel:[0,1,0] op_sel_hi:[0,1,0]
	v_cmp_le_i32_e32 vcc, s17, v86
	s_nor_b64 s[12:13], s[2:3], vcc
	v_add_f32_dpp v28, v28, v28 quad_perm:[1,0,3,2] row_mask:0xf bank_mask:0xf
	v_max_f32_e32 v28, 0xc1200000, v28
	v_min_f32_e32 v28, 0x41200000, v28
	v_mul_f32_e32 v28, 0x3fb8aa3b, v28
	v_exp_f32_e32 v28, v28
	s_nop 0
	v_cndmask_b32_e64 v28, v28, 0, vcc
	s_and_saveexec_b64 s[10:11], s[12:13]
	s_cbranch_execz .LBB1_166
	s_andn2_b64 vcc, exec, s[6:7]
	s_mov_b64 s[12:13], -1
	s_cbranch_vccnz .LBB1_164
	s_mov_b64 s[12:13], 0
	ds_write_b32 v83, v28 offset:256

.LBB1_166:
	s_or_b64 exec, exec, s[10:11]
	s_waitcnt vmcnt(1)
	v_fma_mix_f32 v29, v0, v24, 0 op_sel_hi:[0,1,0]
	v_fma_mix_f32 v24, v1, v24, v29 op_sel:[0,1,0] op_sel_hi:[0,1,0]
	v_fma_mix_f32 v24, v2, v25, v24 op_sel_hi:[0,1,0]
	v_fma_mix_f32 v24, v3, v25, v24 op_sel:[0,1,0] op_sel_hi:[0,1,0]
	v_fma_mix_f32 v24, v4, v26, v24 op_sel_hi:[0,1,0]
	v_fma_mix_f32 v24, v5, v26, v24 op_sel:[0,1,0] op_sel_hi:[0,1,0]
	v_fma_mix_f32 v24, v6, v27, v24 op_sel_hi:[0,1,0]
	v_fma_mix_f32 v24, v7, v27, v24 op_sel:[0,1,0] op_sel_hi:[0,1,0]
	v_cmp_le_i32_e32 vcc, s17, v85
	s_nor_b64 s[12:13], s[2:3], vcc
	v_add_f32_dpp v24, v24, v24 quad_perm:[1,0,3,2] row_mask:0xf bank_mask:0xf
	v_max_f32_e32 v24, 0xc1200000, v24
	v_min_f32_e32 v24, 0x41200000, v24
	v_mul_f32_e32 v24, 0x3fb8aa3b, v24
	v_exp_f32_e32 v24, v24
	s_nop 0
	v_cndmask_b32_e64 v24, v24, 0, vcc
	s_and_saveexec_b64 s[10:11], s[12:13]
	s_cbranch_execz .LBB1_150
	s_andn2_b64 vcc, exec, s[6:7]
	s_mov_b64 s[12:13], -1
	s_cbranch_vccnz .LBB1_169
	s_mov_b64 s[12:13], 0
	ds_write_b32 v83, v24 offset:384
